# attention: resident Q-rope fragments + K-fragment LDS read-ahead deepened to 4 k-steps (4 register sets, uses the freed Q set)
# speedup vs baseline: 1.0042x; 1.0042x over previous
.LBB0_757:
	s_add_i32 s12, s64, -1
	s_sub_i32 s80, s11, 64
	s_cmp_lt_u32 s12, 3
	s_cselect_b32 s80, s10, s80
	s_mul_i32 s81, s80, 0xc00
	s_add_i32 s85, s82, 0x8000
	s_mov_b32 m0, s85
	s_add_i32 s85, s82, 0x10000
	buffer_load_dwordx4 v154, s[72:75], s81 offen lds
	s_mov_b32 m0, s85
	s_add_i32 s85, s82, 0xa000
	buffer_load_dwordx4 v155, s[72:75], s81 offen lds
	s_mov_b32 m0, s85
	s_add_i32 s81, s81, 0x18000
	buffer_load_dwordx4 v154, s[72:75], s81 offen lds
	s_lshl_b32 s81, s83, 11
	s_add_i32 s85, s82, 0x4000
	s_mov_b32 m0, s85
	s_add_i32 s85, s82, 0x6000
	buffer_load_dwordx4 v196, s[76:79], s81 offen lds
	s_mov_b32 m0, s85
	s_add_i32 s81, s81, 0x10000
	buffer_load_dwordx4 v196, s[76:79], s81 offen lds
	s_mov_b32 s84, s80
	s_add_i32 s6, 0, 0x12000
	v_add_u32_e32 v199, s6, v170
	v_add_u32_e32 v204, s6, v171
	v_add_u32_e32 v205, s6, v172
	ds_read_b128 v[64:67], v180 offset:49152
	ds_read_b128 v[68:71], v180 offset:57344
	ds_read_b128 v[200:203], v181 offset:49152
	ds_read_b128 v[226:229], v181 offset:57344
	ds_read_b128 v[230:233], v182 offset:49152
	ds_read_b128 v[234:237], v182 offset:57344
	ds_read_b128 v[238:241], v183 offset:49152
	ds_read_b128 v[242:245], v183 offset:57344
	ds_read_b128 v[246:249], v184 offset:49152
	ds_read_b128 v[250:253], v184 offset:57344
	s_waitcnt lgkmcnt(9)
	v_mfma_f32_32x32x16_bf16 v[80:95], v[64:67], v[124:127], 0
	v_exp_f32_e32 v216, v128
	v_add_f32_e32 v128, 0, v222
	v_add_f32_e32 v128, v224, v128
	v_add_f32_e32 v128, v220, v128
	v_add_f32_e32 v128, v223, v128
	v_add_f32_e32 v128, v219, v128
	v_add_f32_e32 v128, v221, v128
	s_waitcnt lgkmcnt(8)
	v_mfma_f32_32x32x16_bf16 v[64:79], v[68:71], v[124:127], 0
	v_add_f32_e32 v128, v217, v128
	v_add_f32_e32 v128, v218, v128
	v_add_f32_e32 v128, v212, v128
	v_add_f32_e32 v128, v214, v128
	v_add_f32_e32 v128, v211, v128
	v_add_f32_e32 v128, v213, v128
	v_exp_f32_e32 v138, v138
	s_waitcnt lgkmcnt(7)
	v_mfma_f32_32x32x16_bf16 v[80:95], v[200:203], v[120:123], v[80:95]
	v_add_f32_e32 v128, v208, v128
	v_exp_f32_e32 v139, v139
	v_add_f32_e32 v128, v210, v128
	v_exp_f32_e32 v164, v136
	v_add_f32_e32 v128, v207, v128
	v_exp_f32_e32 v137, v137
	v_add_f32_e32 v128, v209, v128
	s_waitcnt lgkmcnt(6)
	v_mfma_f32_32x32x16_bf16 v[64:79], v[226:229], v[120:123], v[64:79]
	ds_read_b128 v[200:203], v185 offset:49152
	ds_read_b128 v[226:229], v185 offset:57344
	v_exp_f32_e32 v165, v132
	v_add_f32_e32 v128, v138, v128
	v_add_f32_e32 v128, v139, v128
	v_exp_f32_e32 v206, v130
	v_add_f32_e32 v128, v164, v128
	v_exp_f32_e32 v215, v131
	s_waitcnt lgkmcnt(7)
	v_mfma_f32_32x32x16_bf16 v[80:95], v[230:233], v[116:119], v[80:95]
	v_add_f32_e32 v128, v137, v128
	v_add_f32_e32 v128, v165, v128
	v_exp_f32_e32 v225, v129
	v_exp_f32_e32 v162, v162
	v_exp_f32_e32 v163, v163
	v_exp_f32_e32 v160, v160
	v_exp_f32_e32 v161, v161
	s_waitcnt lgkmcnt(6)
	v_mfma_f32_32x32x16_bf16 v[64:79], v[234:237], v[116:119], v[64:79]
	ds_read_b128 v[230:233], v186 offset:49152
	ds_read_b128 v[234:237], v186 offset:57344
	v_cvt_pk_bf16_f32 v129, v220, v223
	v_cvt_pk_bf16_f32 v130, v219, v221
	v_cvt_pk_bf16_f32 v131, v217, v218
	v_cvt_pk_bf16_f32 v132, v212, v214
	v_cvt_pk_bf16_f32 v136, v138, v139
	v_cvt_pk_bf16_f32 v137, v164, v137
	s_waitcnt lgkmcnt(7)
	v_mfma_f32_32x32x16_bf16 v[80:95], v[238:241], v[112:115], v[80:95]
	v_cvt_pk_bf16_f32 v139, v206, v215
	v_permlane32_swap_b32_e32 v129, v131
	s_nop 0
	v_permlane32_swap_b32_e32 v137, v139
	s_waitcnt lgkmcnt(6)
	v_mfma_f32_32x32x16_bf16 v[64:79], v[242:245], v[112:115], v[64:79]
	ds_read_b128 v[238:241], v187 offset:49152
	ds_read_b128 v[242:245], v187 offset:57344
	s_waitcnt lgkmcnt(7)
	v_mfma_f32_32x32x16_bf16 v[80:95], v[246:249], v[108:111], v[80:95]
	s_waitcnt lgkmcnt(6)
	v_mfma_f32_32x32x16_bf16 v[64:79], v[250:253], v[108:111], v[64:79]
	ds_read_b128 v[246:249], v199
	ds_read_b128 v[250:253], v199 offset:4096
	s_waitcnt lgkmcnt(7)
	v_mfma_f32_32x32x16_bf16 v[80:95], v[200:203], v[104:107], v[80:95]
	s_waitcnt lgkmcnt(6)
	v_mfma_f32_32x32x16_bf16 v[64:79], v[226:229], v[104:107], v[64:79]
	ds_read_b128 v[200:203], v204
	ds_read_b128 v[226:229], v204 offset:4096
	v_add_u32_e32 v204, s6, v173
	s_waitcnt lgkmcnt(7)
	v_mfma_f32_32x32x16_bf16 v[80:95], v[230:233], v[100:103], v[80:95]
	s_waitcnt lgkmcnt(6)
	v_mfma_f32_32x32x16_bf16 v[64:79], v[234:237], v[100:103], v[64:79]
	ds_read_b128 v[230:233], v205
	ds_read_b128 v[234:237], v205 offset:4096
	s_waitcnt lgkmcnt(7)
	v_mfma_f32_32x32x16_bf16 v[80:95], v[238:241], v[96:99], v[80:95]
	s_waitcnt lgkmcnt(6)
	v_mfma_f32_32x32x16_bf16 v[64:79], v[242:245], v[96:99], v[64:79]
	ds_read_b128 v[238:241], v204
	ds_read_b128 v[242:245], v204 offset:4096
	s_waitcnt lgkmcnt(7)
	v_mfma_f32_32x32x16_bf16 v[80:95], v[246:249], v[142:145], v[80:95]
	s_waitcnt lgkmcnt(6)
	v_mfma_f32_32x32x16_bf16 v[64:79], v[250:253], v[142:145], v[64:79]
	s_waitcnt lgkmcnt(5)
	v_mfma_f32_32x32x16_bf16 v[80:95], v[200:203], v[146:149], v[80:95]
	s_waitcnt lgkmcnt(4)
	v_mfma_f32_32x32x16_bf16 v[64:79], v[226:229], v[146:149], v[64:79]
	s_waitcnt lgkmcnt(3)
	v_mfma_f32_32x32x16_bf16 v[80:95], v[230:233], v[150:153], v[80:95]
	v_exp_f32_e32 v205, v133
	v_cvt_pk_bf16_f32 v133, v211, v213
	v_cvt_pk_bf16_f32 v138, v165, v205
	v_add_f32_e32 v128, v205, v128
	v_add_f32_e32 v128, v206, v128
	v_add_f32_e32 v128, v215, v128
	s_waitcnt lgkmcnt(2)
	v_mfma_f32_32x32x16_bf16 v[64:79], v[234:237], v[150:153], v[64:79]
	v_add_f32_e32 v128, v216, v128
	v_add_f32_e32 v128, v225, v128
	v_add_f32_e32 v128, v162, v128
	v_add_f32_e32 v128, v163, v128
	v_add_f32_e32 v128, v160, v128
	v_add_f32_e32 v128, v161, v128
	s_waitcnt lgkmcnt(1)
	v_mfma_f32_32x32x16_bf16 v[80:95], v[238:241], v[156:159], v[80:95]
	v_exp_f32_e32 v226, v134
	v_exp_f32_e32 v227, v135
	v_cvt_pk_bf16_f32 v134, v208, v210
	v_cvt_pk_bf16_f32 v135, v207, v209
	v_add_f32_e32 v128, v226, v128
	v_add_f32_e32 v203, v227, v128
	v_mov_b32_e32 v204, v203
	s_waitcnt lgkmcnt(0)
	v_mfma_f32_32x32x16_bf16 v[64:79], v[242:245], v[156:159], v[64:79]
	s_nop 0
	v_permlane32_swap_b32_e32 v203, v204
	v_cvt_pk_bf16_f32 v128, v222, v224
	v_cvt_pk_bf16_f32 v208, v216, v225
	v_cvt_pk_bf16_f32 v209, v162, v163
	v_cvt_pk_bf16_f32 v210, v160, v161
	v_cvt_pk_bf16_f32 v211, v226, v227
	v_permlane32_swap_b32_e32 v132, v134
	v_permlane32_swap_b32_e32 v128, v130
	v_permlane32_swap_b32_e32 v133, v135
	v_permlane32_swap_b32_e32 v136, v138
	v_permlane32_swap_b32_e32 v208, v210
	v_permlane32_swap_b32_e32 v209, v211
	ds_read_b64_tr_b16 v[160:161], v167 offset:0
	ds_read_b64_tr_b16 v[162:163], v167 offset:0x800
	ds_read_b64_tr_b16 v[232:233], v167 offset:0x1000
	ds_read_b64_tr_b16 v[234:235], v167 offset:0x1800
	ds_read_b64_tr_b16 v[236:237], v167 offset:0x2000
	ds_read_b64_tr_b16 v[238:239], v167 offset:0x2800
	ds_read_b64_tr_b16 v[240:241], v167 offset:0x3000
	ds_read_b64_tr_b16 v[242:243], v167 offset:0x3800
	v_max_f32_e32 v164, v81, v81
	v_max_f32_e32 v165, v80, v80
	v_max_f32_e32 v164, v165, v164
	v_max3_f32 v164, v164, v82, v83
	v_max3_f32 v164, v164, v84, v85
	v_max3_f32 v164, v164, v86, v87
	v_max3_f32 v164, v164, v88, v89
	v_max3_f32 v164, v164, v90, v91
	v_max3_f32 v164, v164, v92, v93
	v_max3_f32 v164, v164, v94, v95
	s_waitcnt lgkmcnt(0)
	v_mfma_f32_32x32x16_bf16 v[16:31], v[128:131], v[160:163], v[16:31]
	v_max3_f32 v160, v164, v64, v65
	v_max3_f32 v160, v160, v66, v67
	v_max3_f32 v160, v160, v68, v69
	v_mfma_f32_32x32x16_bf16 v[16:31], v[132:135], v[232:235], v[16:31]
	ds_read_b64_tr_b16 v[232:233], v167 offset:0x200
	ds_read_b64_tr_b16 v[234:235], v167 offset:0xa00
	v_max3_f32 v160, v160, v70, v71
	v_max3_f32 v160, v160, v72, v73
	v_max3_f32 v160, v160, v74, v75
	v_mfma_f32_32x32x16_bf16 v[16:31], v[136:139], v[236:239], v[16:31]
	ds_read_b64_tr_b16 v[236:237], v167 offset:0x1200
	ds_read_b64_tr_b16 v[238:239], v167 offset:0x1a00
	ds_read_b64_tr_b16 v[244:245], v167 offset:0x2200
	ds_read_b64_tr_b16 v[246:247], v167 offset:0x2a00
	ds_read_b64_tr_b16 v[248:249], v167 offset:0x3200
	ds_read_b64_tr_b16 v[250:251], v167 offset:0x3a00
	v_max3_f32 v160, v160, v76, v77
	v_max3_f32 v160, v160, v78, v79
	v_mov_b32_e32 v161, v160
	v_mfma_f32_32x32x16_bf16 v[16:31], v[208:211], v[240:243], v[16:31]
	v_max_f32_e32 v162, v198, v198
	v_permlane32_swap_b32_e32 v160, v161
	v_max_f32_e32 v161, v161, v161
	v_max_f32_e32 v160, v160, v160
	v_max_f32_e32 v160, v160, v161
	s_waitcnt lgkmcnt(0)
	v_mfma_f32_32x32x16_bf16 v[32:47], v[128:131], v[232:235], v[32:47]
	ds_read_b64_tr_b16 v[232:233], v167 offset:0x400
	ds_read_b64_tr_b16 v[234:235], v167 offset:0xc00
	v_sub_f32_e32 v161, v160, v198
	v_max_f32_e32 v160, v162, v160
	v_sub_f32_e32 v162, v198, v160
	v_mul_f32_e32 v162, 0x3dd53b94, v162
	v_exp_f32_e32 v162, v162
	v_mfma_f32_32x32x16_bf16 v[32:47], v[132:135], v[236:239], v[32:47]
	ds_read_b64_tr_b16 v[236:237], v167 offset:0x1400
	ds_read_b64_tr_b16 v[238:239], v167 offset:0x1c00
	ds_read_b64_tr_b16 v[240:241], v167 offset:0x2400
	ds_read_b64_tr_b16 v[242:243], v167 offset:0x2c00
	v_cmp_ge_f32_e32 vcc, s48, v161
	s_cmp_eq_u64 vcc, exec
	s_cselect_b64 s[6:7], -1, 0
	v_cndmask_b32_e64 v206, v162, 1.0, s[6:7]
	v_cndmask_b32_e64 v160, v160, v198, s[6:7]
	v_mul_f32_e32 v205, 0xbdd53b94, v160
	v_cmp_gt_f32_e32 vcc, 1.0, v206
	v_mfma_f32_32x32x16_bf16 v[32:47], v[136:139], v[244:247], v[32:47]
	ds_read_b64_tr_b16 v[244:245], v167 offset:0x3400
	ds_read_b64_tr_b16 v[246:247], v167 offset:0x3c00
	v_fmamk_f32 v87, v87, 0x3dd53b94, v205
	v_fmamk_f32 v80, v80, 0x3dd53b94, v205
	v_fmamk_f32 v81, v81, 0x3dd53b94, v205
	v_fmamk_f32 v82, v82, 0x3dd53b94, v205
	v_fmamk_f32 v83, v83, 0x3dd53b94, v205
	v_mfma_f32_32x32x16_bf16 v[32:47], v[208:211], v[248:251], v[32:47]
	v_fmamk_f32 v84, v84, 0x3dd53b94, v205
	v_fmamk_f32 v85, v85, 0x3dd53b94, v205
	v_fmamk_f32 v86, v86, 0x3dd53b94, v205
	v_fmamk_f32 v88, v88, 0x3dd53b94, v205
	v_fmamk_f32 v89, v89, 0x3dd53b94, v205
	s_waitcnt lgkmcnt(0)
	v_mfma_f32_32x32x16_bf16 v[0:15], v[128:131], v[232:235], v[0:15]
	ds_read_b64_tr_b16 v[232:233], v167 offset:0x600
	ds_read_b64_tr_b16 v[234:235], v167 offset:0xe00
	v_fmamk_f32 v90, v90, 0x3dd53b94, v205
	v_fmamk_f32 v91, v91, 0x3dd53b94, v205
	v_fmamk_f32 v92, v92, 0x3dd53b94, v205
	v_fmamk_f32 v93, v93, 0x3dd53b94, v205
	v_fmamk_f32 v94, v94, 0x3dd53b94, v205
	v_mfma_f32_32x32x16_bf16 v[0:15], v[132:135], v[236:239], v[0:15]
	ds_read_b64_tr_b16 v[236:237], v167 offset:0x1600
	ds_read_b64_tr_b16 v[238:239], v167 offset:0x1e00
	v_fmamk_f32 v95, v95, 0x3dd53b94, v205
	v_fmamk_f32 v215, v64, 0x3dd53b94, v205
	v_fmamk_f32 v216, v65, 0x3dd53b94, v205
	v_fmamk_f32 v217, v66, 0x3dd53b94, v205
	v_fmamk_f32 v218, v67, 0x3dd53b94, v205
	v_mfma_f32_32x32x16_bf16 v[0:15], v[136:139], v[240:243], v[0:15]
	ds_read_b64_tr_b16 v[240:241], v167 offset:0x2600
	ds_read_b64_tr_b16 v[242:243], v167 offset:0x2e00
	ds_read_b64_tr_b16 v[248:249], v167 offset:0x3600
	ds_read_b64_tr_b16 v[250:251], v167 offset:0x3e00
	v_fmamk_f32 v219, v68, 0x3dd53b94, v205
	v_fmamk_f32 v212, v73, 0x3dd53b94, v205
	v_fmamk_f32 v213, v74, 0x3dd53b94, v205
	v_fmamk_f32 v214, v75, 0x3dd53b94, v205
	v_mfma_f32_32x32x16_bf16 v[0:15], v[208:211], v[244:247], v[0:15]
	v_fmamk_f32 v207, v76, 0x3dd53b94, v205
	v_fmamk_f32 v220, v77, 0x3dd53b94, v205
	v_fmamk_f32 v221, v78, 0x3dd53b94, v205
	s_waitcnt lgkmcnt(0)
	v_mfma_f32_32x32x16_bf16 v[48:63], v[128:131], v[232:235], v[48:63]
	v_exp_f32_e32 v128, v80
	v_exp_f32_e32 v129, v82
	v_exp_f32_e32 v130, v84
	v_exp_f32_e32 v131, v86
	v_mfma_f32_32x32x16_bf16 v[48:63], v[132:135], v[236:239], v[48:63]
	v_exp_f32_e32 v132, v88
	v_exp_f32_e32 v133, v90
	v_exp_f32_e32 v134, v92
	v_exp_f32_e32 v135, v94
	v_mfma_f32_32x32x16_bf16 v[48:63], v[136:139], v[240:243], v[48:63]
	v_exp_f32_e32 v139, v89
	v_exp_f32_e32 v138, v91
	v_exp_f32_e32 v137, v93
	v_exp_f32_e32 v136, v95
	v_mfma_f32_32x32x16_bf16 v[48:63], v[208:211], v[248:251], v[48:63]
	v_exp_f32_e32 v161, v87
	v_exp_f32_e32 v198, v81
	v_exp_f32_e32 v163, v83
	v_exp_f32_e32 v162, v85
	v_fmamk_f32 v208, v69, 0x3dd53b94, v205
	v_fmamk_f32 v209, v70, 0x3dd53b94, v205
	v_fmamk_f32 v210, v71, 0x3dd53b94, v205
	v_fmamk_f32 v211, v72, 0x3dd53b94, v205
	v_fmac_f32_e32 v205, 0x3dd53b94, v79
	s_cbranch_vccz .LBB0_761
	s_and_saveexec_b64 s[8:9], s[4:5]
	ds_write_b32 v189, v206 offset:128
	s_or_b64 exec, exec, s[8:9]
	s_waitcnt lgkmcnt(0)
	v_add_u32_e32 v248, s62, v169
	ds_read_b128 v[232:235], v248 offset:224
	ds_read_b128 v[236:239], v248 offset:192
	ds_read_b128 v[240:243], v248 offset:160
	ds_read_b128 v[244:247], v248 offset:128
	s_waitcnt lgkmcnt(3)
	v_pk_mul_f32 v[28:29], v[28:29], v[232:233]
	s_waitcnt lgkmcnt(2)
	v_pk_mul_f32 v[24:25], v[24:25], v[236:237]
	s_waitcnt lgkmcnt(1)
	v_pk_mul_f32 v[20:21], v[20:21], v[240:241]
	v_pk_mul_f32 v[30:31], v[30:31], v[234:235]
	v_pk_mul_f32 v[26:27], v[26:27], v[238:239]
	v_pk_mul_f32 v[22:23], v[22:23], v[242:243]
	s_waitcnt lgkmcnt(0)
	v_pk_mul_f32 v[18:19], v[18:19], v[246:247]
	v_pk_mul_f32 v[16:17], v[16:17], v[244:245]
	v_pk_mul_f32 v[44:45], v[44:45], v[232:233]
	v_pk_mul_f32 v[40:41], v[40:41], v[236:237]
	v_pk_mul_f32 v[36:37], v[36:37], v[240:241]
	v_pk_mul_f32 v[46:47], v[46:47], v[234:235]
	v_pk_mul_f32 v[42:43], v[42:43], v[238:239]
	v_pk_mul_f32 v[38:39], v[38:39], v[242:243]
	v_pk_mul_f32 v[34:35], v[34:35], v[246:247]
	v_pk_mul_f32 v[32:33], v[32:33], v[244:245]
	v_pk_mul_f32 v[12:13], v[12:13], v[232:233]
	v_pk_mul_f32 v[8:9], v[8:9], v[236:237]
	v_pk_mul_f32 v[4:5], v[4:5], v[240:241]
	v_pk_mul_f32 v[14:15], v[14:15], v[234:235]
	v_pk_mul_f32 v[10:11], v[10:11], v[238:239]
	v_pk_mul_f32 v[6:7], v[6:7], v[242:243]
	v_pk_mul_f32 v[2:3], v[2:3], v[246:247]
	v_pk_mul_f32 v[0:1], v[0:1], v[244:245]
	v_pk_mul_f32 v[60:61], v[60:61], v[232:233]
	v_pk_mul_f32 v[56:57], v[56:57], v[236:237]
	v_pk_mul_f32 v[52:53], v[52:53], v[240:241]
	v_pk_mul_f32 v[62:63], v[62:63], v[234:235]
	v_pk_mul_f32 v[58:59], v[58:59], v[238:239]
	v_pk_mul_f32 v[54:55], v[54:55], v[242:243]
	v_pk_mul_f32 v[50:51], v[50:51], v[246:247]
	v_pk_mul_f32 v[48:49], v[48:49], v[244:245]
.LBB0_761:
	s_waitcnt vmcnt(0) lgkmcnt(0)
	s_barrier
	s_add_i32 s80, s10, 64
	s_cmp_lt_u32 s12, 2
	s_cselect_b32 s80, s80, s11
	s_mul_i32 s81, s80, 0xc00
	s_add_i32 s85, s82, 0xc000
	s_mov_b32 m0, s85
	s_add_i32 s85, s82, 0x12000
	buffer_load_dwordx4 v154, s[72:75], s81 offen lds
	s_mov_b32 m0, s85
	s_add_i32 s85, s82, 0xe000
	buffer_load_dwordx4 v155, s[72:75], s81 offen lds
	s_mov_b32 m0, s85
	s_add_i32 s81, s81, 0x18000
	buffer_load_dwordx4 v154, s[72:75], s81 offen lds
	s_lshl_b32 s81, s84, 11
	s_add_i32 s85, s82, 0x0
	s_mov_b32 m0, s85
	s_add_i32 s85, s82, 0x2000
	buffer_load_dwordx4 v196, s[76:79], s81 offen lds
	s_mov_b32 m0, s85
	s_add_i32 s81, s81, 0x10000
	buffer_load_dwordx4 v196, s[76:79], s81 offen lds
	s_mov_b32 s83, s80
	ds_read_b128 v[64:67], v180 offset:32768
	ds_read_b128 v[68:71], v180 offset:40960
	ds_read_b128 v[222:225], v181 offset:32768
	ds_read_b128 v[226:229], v181 offset:40960
	ds_read_b128 v[230:233], v182 offset:32768
	ds_read_b128 v[234:237], v182 offset:40960
	ds_read_b128 v[238:241], v183 offset:32768
	ds_read_b128 v[242:245], v183 offset:40960
	ds_read_b128 v[246:249], v184 offset:32768
	ds_read_b128 v[250:253], v184 offset:40960
	v_exp_f32_e32 v164, v215
	v_add_f32_e32 v215, 0, v128
	s_waitcnt lgkmcnt(9)
	v_mfma_f32_32x32x16_bf16 v[80:95], v[64:67], v[124:127], 0
	v_add_f32_e32 v215, v198, v215
	v_add_f32_e32 v215, v129, v215
	v_add_f32_e32 v215, v163, v215
	v_add_f32_e32 v215, v130, v215
	v_add_f32_e32 v215, v162, v215
	v_add_f32_e32 v215, v131, v215
	v_add_f32_e32 v215, v161, v215
	s_waitcnt lgkmcnt(8)
	v_mfma_f32_32x32x16_bf16 v[64:79], v[68:71], v[124:127], 0
	v_add_f32_e32 v215, v132, v215
	v_add_f32_e32 v215, v139, v215
	v_add_f32_e32 v215, v133, v215
	v_add_f32_e32 v215, v138, v215
	v_add_f32_e32 v215, v134, v215
	v_exp_f32_e32 v165, v216
	v_add_f32_e32 v215, v137, v215
	s_waitcnt lgkmcnt(7)
	v_mfma_f32_32x32x16_bf16 v[80:95], v[222:225], v[120:123], v[80:95]
	v_exp_f32_e32 v217, v217
	v_add_f32_e32 v215, v135, v215
	v_exp_f32_e32 v218, v218
	v_add_f32_e32 v215, v136, v215
	v_exp_f32_e32 v219, v219
	v_add_f32_e32 v215, v164, v215
	v_exp_f32_e32 v208, v208
	s_waitcnt lgkmcnt(6)
	v_mfma_f32_32x32x16_bf16 v[64:79], v[226:229], v[120:123], v[64:79]
	ds_read_b128 v[222:225], v185 offset:32768
	ds_read_b128 v[226:229], v185 offset:40960
	v_add_f32_e32 v215, v165, v215
	v_exp_f32_e32 v209, v209
	v_add_f32_e32 v215, v217, v215
	v_exp_f32_e32 v210, v210
	v_add_f32_e32 v215, v218, v215
	v_exp_f32_e32 v211, v211
	s_waitcnt lgkmcnt(7)
	v_mfma_f32_32x32x16_bf16 v[80:95], v[230:233], v[116:119], v[80:95]
	v_add_f32_e32 v215, v219, v215
	v_exp_f32_e32 v212, v212
	v_add_f32_e32 v215, v208, v215
	v_exp_f32_e32 v213, v213
	v_add_f32_e32 v215, v209, v215
	v_exp_f32_e32 v214, v214
	v_add_f32_e32 v215, v210, v215
	s_waitcnt lgkmcnt(6)
	v_mfma_f32_32x32x16_bf16 v[64:79], v[234:237], v[116:119], v[64:79]
	ds_read_b128 v[230:233], v186 offset:32768
	ds_read_b128 v[234:237], v186 offset:40960
	v_exp_f32_e32 v207, v207
	v_add_f32_e32 v215, v211, v215
	v_exp_f32_e32 v220, v220
	v_add_f32_e32 v215, v212, v215
	v_exp_f32_e32 v221, v221
	v_add_f32_e32 v215, v213, v215
	s_waitcnt lgkmcnt(7)
	v_mfma_f32_32x32x16_bf16 v[80:95], v[238:241], v[112:115], v[80:95]
	v_exp_f32_e32 v205, v205
	v_add_f32_e32 v215, v214, v215
	v_add_f32_e32 v215, v207, v215
	v_add_f32_e32 v215, v220, v215
	v_add_f32_e32 v215, v221, v215
	v_add_f32_e32 v215, v205, v215
	v_mov_b32_e32 v216, v215
	s_waitcnt lgkmcnt(6)
	v_mfma_f32_32x32x16_bf16 v[64:79], v[242:245], v[112:115], v[64:79]
	ds_read_b128 v[238:241], v187 offset:32768
	ds_read_b128 v[242:245], v187 offset:40960
	v_permlane32_swap_b32_e32 v215, v216
	v_cvt_pk_bf16_f32 v128, v128, v198
	v_cvt_pk_bf16_f32 v129, v129, v163
	v_cvt_pk_bf16_f32 v130, v130, v162
	v_cvt_pk_bf16_f32 v131, v131, v161
	s_waitcnt lgkmcnt(7)
	v_mfma_f32_32x32x16_bf16 v[80:95], v[246:249], v[108:111], v[80:95]
	v_cvt_pk_bf16_f32 v132, v132, v139
	v_cvt_pk_bf16_f32 v133, v133, v138
	v_cvt_pk_bf16_f32 v134, v134, v137
	v_cvt_pk_bf16_f32 v135, v135, v136
	v_cvt_pk_bf16_f32 v136, v164, v165
	v_cvt_pk_bf16_f32 v137, v217, v218
	v_cvt_pk_bf16_f32 v138, v219, v208
	s_waitcnt lgkmcnt(6)
	v_mfma_f32_32x32x16_bf16 v[64:79], v[250:253], v[108:111], v[64:79]
	ds_read_b128 v[246:249], v191
	ds_read_b128 v[250:253], v191 offset:4096
	v_cvt_pk_bf16_f32 v139, v209, v210
	v_cvt_pk_bf16_f32 v208, v211, v212
	v_cvt_pk_bf16_f32 v209, v213, v214
	v_cvt_pk_bf16_f32 v210, v207, v220
	v_cvt_pk_bf16_f32 v211, v221, v205
	v_permlane32_swap_b32_e32 v128, v130
	s_waitcnt lgkmcnt(7)
	v_mfma_f32_32x32x16_bf16 v[80:95], v[222:225], v[104:107], v[80:95]
	v_permlane32_swap_b32_e32 v129, v131
	v_permlane32_swap_b32_e32 v132, v134
	v_permlane32_swap_b32_e32 v133, v135
	v_permlane32_swap_b32_e32 v136, v138
	s_waitcnt lgkmcnt(6)
	v_mfma_f32_32x32x16_bf16 v[64:79], v[226:229], v[104:107], v[64:79]
	ds_read_b128 v[222:225], v192
	ds_read_b128 v[226:229], v192 offset:4096
	v_permlane32_swap_b32_e32 v137, v139
	v_permlane32_swap_b32_e32 v208, v210
	v_permlane32_swap_b32_e32 v209, v211
	s_waitcnt lgkmcnt(7)
	v_mfma_f32_32x32x16_bf16 v[80:95], v[230:233], v[100:103], v[80:95]
	s_waitcnt lgkmcnt(6)
	v_mfma_f32_32x32x16_bf16 v[64:79], v[234:237], v[100:103], v[64:79]
	ds_read_b128 v[230:233], v193
	ds_read_b128 v[234:237], v193 offset:4096
	s_waitcnt lgkmcnt(7)
	v_mfma_f32_32x32x16_bf16 v[80:95], v[238:241], v[96:99], v[80:95]
	s_waitcnt lgkmcnt(6)
	v_mfma_f32_32x32x16_bf16 v[64:79], v[242:245], v[96:99], v[64:79]
	ds_read_b128 v[238:241], v194
	ds_read_b128 v[242:245], v194 offset:4096
	s_waitcnt lgkmcnt(7)
	v_mfma_f32_32x32x16_bf16 v[80:95], v[246:249], v[142:145], v[80:95]
	s_waitcnt lgkmcnt(6)
	v_mfma_f32_32x32x16_bf16 v[64:79], v[250:253], v[142:145], v[64:79]
	s_waitcnt lgkmcnt(5)
	v_mfma_f32_32x32x16_bf16 v[80:95], v[222:225], v[146:149], v[80:95]
	s_waitcnt lgkmcnt(4)
	v_mfma_f32_32x32x16_bf16 v[64:79], v[226:229], v[146:149], v[64:79]
	s_waitcnt lgkmcnt(3)
	v_mfma_f32_32x32x16_bf16 v[80:95], v[230:233], v[150:153], v[80:95]
	s_waitcnt lgkmcnt(2)
	v_mfma_f32_32x32x16_bf16 v[64:79], v[234:237], v[150:153], v[64:79]
	s_waitcnt lgkmcnt(1)
	v_mfma_f32_32x32x16_bf16 v[80:95], v[238:241], v[156:159], v[80:95]
	s_waitcnt lgkmcnt(0)
	v_mfma_f32_32x32x16_bf16 v[64:79], v[242:245], v[156:159], v[64:79]
	ds_read_b64_tr_b16 v[238:239], v174 offset:0
	ds_read_b64_tr_b16 v[240:241], v174 offset:0x800
	ds_read_b64_tr_b16 v[242:243], v174 offset:0x1000
	ds_read_b64_tr_b16 v[244:245], v174 offset:0x1800
	ds_read_b64_tr_b16 v[246:247], v174 offset:0x2000
	ds_read_b64_tr_b16 v[248:249], v174 offset:0x2800
	ds_read_b64_tr_b16 v[250:251], v174 offset:0x3000
	ds_read_b64_tr_b16 v[252:253], v174 offset:0x3800
	s_nop 3
	v_max_f32_e32 v161, v81, v81
	v_max_f32_e32 v162, v80, v80
	v_max_f32_e32 v161, v162, v161
	v_max3_f32 v161, v161, v82, v83
	v_max3_f32 v161, v161, v84, v85
	v_max3_f32 v161, v161, v86, v87
	v_max3_f32 v161, v161, v88, v89
	v_max3_f32 v161, v161, v90, v91
	v_max3_f32 v161, v161, v92, v93
	v_max3_f32 v161, v161, v94, v95
	s_waitcnt lgkmcnt(0)
	v_mfma_f32_32x32x16_bf16 v[16:31], v[128:131], v[238:241], v[16:31]
	ds_read_b64_tr_b16 v[238:239], v174 offset:0x200
	ds_read_b64_tr_b16 v[240:241], v174 offset:0xa00
	v_max3_f32 v161, v161, v64, v65
	v_max3_f32 v161, v161, v66, v67
	v_max3_f32 v161, v161, v68, v69
	v_mfma_f32_32x32x16_bf16 v[16:31], v[132:135], v[242:245], v[16:31]
	ds_read_b64_tr_b16 v[242:243], v174 offset:0x1200
	ds_read_b64_tr_b16 v[244:245], v174 offset:0x1a00
	v_max3_f32 v161, v161, v70, v71
	v_max3_f32 v161, v161, v72, v73
	v_max3_f32 v161, v161, v74, v75
	v_mfma_f32_32x32x16_bf16 v[16:31], v[136:139], v[246:249], v[16:31]
	ds_read_b64_tr_b16 v[246:247], v174 offset:0x2200
	ds_read_b64_tr_b16 v[248:249], v174 offset:0x2a00
	ds_read_b64_tr_b16 v[162:163], v174 offset:0x3200
	ds_read_b64_tr_b16 v[164:165], v174 offset:0x3a00
	v_max3_f32 v161, v161, v76, v77
	v_max3_f32 v161, v161, v78, v79
	v_mov_b32_e32 v198, v161
	v_mfma_f32_32x32x16_bf16 v[16:31], v[208:211], v[250:253], v[16:31]
	v_max_f32_e32 v205, v160, v160
	v_permlane32_swap_b32_e32 v161, v198
	v_max_f32_e32 v198, v198, v198
	v_max_f32_e32 v161, v161, v161
	v_max_f32_e32 v161, v161, v198
	s_waitcnt lgkmcnt(0)
	v_mfma_f32_32x32x16_bf16 v[32:47], v[128:131], v[238:241], v[32:47]
	ds_read_b64_tr_b16 v[238:239], v174 offset:0x400
	ds_read_b64_tr_b16 v[240:241], v174 offset:0xc00
	v_sub_f32_e32 v198, v161, v160
	v_max_f32_e32 v161, v205, v161
	v_sub_f32_e32 v205, v160, v161
	v_mul_f32_e32 v205, 0x3dd53b94, v205
	v_exp_f32_e32 v205, v205
	v_mfma_f32_32x32x16_bf16 v[32:47], v[132:135], v[242:245], v[32:47]
	ds_read_b64_tr_b16 v[242:243], v174 offset:0x1400
	ds_read_b64_tr_b16 v[244:245], v174 offset:0x1c00
	v_cmp_ge_f32_e32 vcc, s48, v198
	s_cmp_eq_u64 vcc, exec
	s_cselect_b64 s[6:7], -1, 0
	v_cndmask_b32_e64 v205, v205, 1.0, s[6:7]
	v_cndmask_b32_e64 v198, v161, v160, s[6:7]
	v_mul_f32_e32 v236, 0xbdd53b94, v198
	v_mov_b32_e32 v237, v236
	v_cmp_gt_f32_e32 vcc, 1.0, v205
	v_mfma_f32_32x32x16_bf16 v[32:47], v[136:139], v[246:249], v[32:47]
	ds_read_b64_tr_b16 v[246:247], v174 offset:0x2400
	ds_read_b64_tr_b16 v[248:249], v174 offset:0x2c00
	ds_read_b64_tr_b16 v[250:251], v174 offset:0x3400
	ds_read_b64_tr_b16 v[252:253], v174 offset:0x3c00
	v_fmamk_f32 v80, v80, 0x3dd53b94, v236
	v_fmamk_f32 v81, v81, 0x3dd53b94, v236
	v_fmamk_f32 v82, v82, 0x3dd53b94, v236
	v_fmamk_f32 v83, v83, 0x3dd53b94, v236
	v_mfma_f32_32x32x16_bf16 v[32:47], v[208:211], v[162:165], v[32:47]
	v_fmamk_f32 v84, v84, 0x3dd53b94, v236
	v_fmamk_f32 v85, v85, 0x3dd53b94, v236
	v_fmamk_f32 v86, v86, 0x3dd53b94, v236
	v_fmamk_f32 v87, v87, 0x3dd53b94, v236
	s_waitcnt lgkmcnt(0)
	v_mfma_f32_32x32x16_bf16 v[0:15], v[128:131], v[238:241], v[0:15]
	ds_read_b64_tr_b16 v[162:163], v174 offset:0x600
	ds_read_b64_tr_b16 v[164:165], v174 offset:0xe00
	ds_read_b64_tr_b16 v[238:239], v174 offset:0x1600
	ds_read_b64_tr_b16 v[240:241], v174 offset:0x1e00
	v_fmamk_f32 v88, v88, 0x3dd53b94, v236
	v_fmamk_f32 v89, v89, 0x3dd53b94, v236
	v_fmamk_f32 v90, v90, 0x3dd53b94, v236
	v_fmamk_f32 v91, v91, 0x3dd53b94, v236
	v_mfma_f32_32x32x16_bf16 v[0:15], v[132:135], v[242:245], v[0:15]
	ds_read_b64_tr_b16 v[242:243], v174 offset:0x2600
	ds_read_b64_tr_b16 v[244:245], v174 offset:0x2e00
	v_fmamk_f32 v92, v92, 0x3dd53b94, v236
	v_fmamk_f32 v93, v93, 0x3dd53b94, v236
	v_fmamk_f32 v94, v94, 0x3dd53b94, v236
	v_fmamk_f32 v95, v95, 0x3dd53b94, v236
	v_mfma_f32_32x32x16_bf16 v[0:15], v[136:139], v[246:249], v[0:15]
	ds_read_b64_tr_b16 v[246:247], v174 offset:0x3600
	ds_read_b64_tr_b16 v[248:249], v174 offset:0x3e00
	v_exp_f32_e32 v222, v80
	v_exp_f32_e32 v224, v81
	v_exp_f32_e32 v220, v82
	v_mfma_f32_32x32x16_bf16 v[0:15], v[208:211], v[250:253], v[0:15]
	v_exp_f32_e32 v223, v83
	v_exp_f32_e32 v219, v84
	v_exp_f32_e32 v221, v85
	s_waitcnt lgkmcnt(0)
	v_mfma_f32_32x32x16_bf16 v[48:63], v[128:131], v[162:165], v[48:63]
	v_exp_f32_e32 v217, v86
	v_exp_f32_e32 v218, v87
	v_exp_f32_e32 v212, v88
	v_pk_fma_f32 v[130:131], v[70:71], s[28:29], v[236:237] op_sel_hi:[1,0,0]
	v_pk_fma_f32 v[128:129], v[72:73], s[28:29], v[236:237] op_sel_hi:[1,0,0]
	v_mfma_f32_32x32x16_bf16 v[48:63], v[132:135], v[238:241], v[48:63]
	v_exp_f32_e32 v214, v89
	v_exp_f32_e32 v213, v91
	v_exp_f32_e32 v207, v94
	v_pk_fma_f32 v[132:133], v[68:69], s[28:29], v[236:237] op_sel_hi:[1,0,0]
	v_pk_fma_f32 v[134:135], v[78:79], s[28:29], v[236:237] op_sel_hi:[1,0,0]
	v_mfma_f32_32x32x16_bf16 v[48:63], v[136:139], v[242:245], v[48:63]
	v_pk_fma_f32 v[138:139], v[64:65], s[28:29], v[236:237] op_sel_hi:[1,0,0]
	v_pk_fma_f32 v[136:137], v[66:67], s[28:29], v[236:237] op_sel_hi:[1,0,0]
	v_pk_fma_f32 v[162:163], v[74:75], s[28:29], v[236:237] op_sel_hi:[1,0,0]
	v_pk_fma_f32 v[160:161], v[76:77], s[28:29], v[236:237] op_sel_hi:[1,0,0]
	v_mfma_f32_32x32x16_bf16 v[48:63], v[208:211], v[246:249], v[48:63]
	v_exp_f32_e32 v211, v90
	v_exp_f32_e32 v208, v92
	v_exp_f32_e32 v210, v93
	v_exp_f32_e32 v209, v95
	v_add_f32_e32 v64, v203, v204
	v_fmac_f32_e32 v64, v197, v140
	v_add_f32_e32 v140, v215, v216
	s_addk_i32 s10, 0x80
	s_add_i32 s64, s64, 2
	s_addk_i32 s11, 0x80
	v_fmac_f32_e32 v140, v64, v206
	s_cbranch_vccz .LBB0_765
	s_and_saveexec_b64 s[8:9], s[4:5]
	ds_write_b32 v189, v205 offset:128
	s_or_b64 exec, exec, s[8:9]
	s_waitcnt lgkmcnt(0)
	v_add_u32_e32 v164, s62, v169
	ds_read_b128 v[238:241], v164 offset:224
	ds_read_b128 v[242:245], v164 offset:192
	ds_read_b128 v[246:249], v164 offset:160
	ds_read_b128 v[250:253], v164 offset:128
	s_waitcnt lgkmcnt(3)
	v_pk_mul_f32 v[28:29], v[28:29], v[238:239]
	s_waitcnt lgkmcnt(2)
	v_pk_mul_f32 v[24:25], v[24:25], v[242:243]
	s_waitcnt lgkmcnt(1)
	v_pk_mul_f32 v[20:21], v[20:21], v[246:247]
	v_pk_mul_f32 v[30:31], v[30:31], v[240:241]
	v_pk_mul_f32 v[26:27], v[26:27], v[244:245]
	v_pk_mul_f32 v[22:23], v[22:23], v[248:249]
	s_waitcnt lgkmcnt(0)
	v_pk_mul_f32 v[18:19], v[18:19], v[252:253]
	v_pk_mul_f32 v[16:17], v[16:17], v[250:251]
	v_pk_mul_f32 v[44:45], v[44:45], v[238:239]
	v_pk_mul_f32 v[40:41], v[40:41], v[242:243]
	v_pk_mul_f32 v[36:37], v[36:37], v[246:247]
	v_pk_mul_f32 v[46:47], v[46:47], v[240:241]
	v_pk_mul_f32 v[42:43], v[42:43], v[244:245]
	v_pk_mul_f32 v[38:39], v[38:39], v[248:249]
	v_pk_mul_f32 v[34:35], v[34:35], v[252:253]
	v_pk_mul_f32 v[32:33], v[32:33], v[250:251]
	v_pk_mul_f32 v[12:13], v[12:13], v[238:239]
	v_pk_mul_f32 v[8:9], v[8:9], v[242:243]
	v_pk_mul_f32 v[4:5], v[4:5], v[246:247]
	v_pk_mul_f32 v[14:15], v[14:15], v[240:241]
	v_pk_mul_f32 v[10:11], v[10:11], v[244:245]
	v_pk_mul_f32 v[6:7], v[6:7], v[248:249]
	v_pk_mul_f32 v[2:3], v[2:3], v[252:253]
	v_pk_mul_f32 v[0:1], v[0:1], v[250:251]
	v_pk_mul_f32 v[60:61], v[60:61], v[238:239]
	v_pk_mul_f32 v[56:57], v[56:57], v[242:243]
	v_pk_mul_f32 v[52:53], v[52:53], v[246:247]
	v_pk_mul_f32 v[62:63], v[62:63], v[240:241]
	v_pk_mul_f32 v[58:59], v[58:59], v[244:245]
	v_pk_mul_f32 v[54:55], v[54:55], v[248:249]
	v_pk_mul_f32 v[50:51], v[50:51], v[252:253]
	v_pk_mul_f32 v[48:49], v[48:49], v[250:251]

.LBB0_2012:
	s_add_i32 s8, s8, 2
	s_sub_i32 s80, s14, 64
	s_cmp_lt_u32 s8, 3
	s_cselect_b32 s80, s13, s80
	s_mul_i32 s81, s80, 0xc00
	s_add_i32 s85, s82, 0x8000
	s_mov_b32 m0, s85
	s_add_i32 s85, s82, 0x10000
	buffer_load_dwordx4 v154, s[72:75], s81 offen lds
	s_mov_b32 m0, s85
	s_add_i32 s85, s82, 0xa000
	buffer_load_dwordx4 v155, s[72:75], s81 offen lds
	s_mov_b32 m0, s85
	s_add_i32 s81, s81, 0x18000
	buffer_load_dwordx4 v154, s[72:75], s81 offen lds
	s_lshl_b32 s81, s83, 11
	s_add_i32 s85, s82, 0x4000
	s_mov_b32 m0, s85
	s_add_i32 s85, s82, 0x6000
	buffer_load_dwordx4 v196, s[76:79], s81 offen lds
	s_mov_b32 m0, s85
	s_add_i32 s81, s81, 0x10000
	buffer_load_dwordx4 v196, s[76:79], s81 offen lds
	s_mov_b32 s84, s80
	s_add_i32 s6, 0, 0x12000
	v_add_u32_e32 v199, s6, v170
	v_add_u32_e32 v204, s6, v171
	v_add_u32_e32 v205, s6, v172
	ds_read_b128 v[64:67], v180 offset:49152
	ds_read_b128 v[68:71], v180 offset:57344
	ds_read_b128 v[200:203], v181 offset:49152
	ds_read_b128 v[226:229], v181 offset:57344
	ds_read_b128 v[230:233], v182 offset:49152
	ds_read_b128 v[234:237], v182 offset:57344
	ds_read_b128 v[238:241], v183 offset:49152
	ds_read_b128 v[242:245], v183 offset:57344
	ds_read_b128 v[246:249], v184 offset:49152
	ds_read_b128 v[250:253], v184 offset:57344
	s_waitcnt lgkmcnt(9)
	v_mfma_f32_32x32x16_bf16 v[80:95], v[64:67], v[124:127], 0
	v_exp_f32_e32 v216, v128
	v_add_f32_e32 v128, 0, v222
	v_add_f32_e32 v128, v224, v128
	v_add_f32_e32 v128, v220, v128
	v_add_f32_e32 v128, v223, v128
	v_add_f32_e32 v128, v219, v128
	v_add_f32_e32 v128, v221, v128
	s_waitcnt lgkmcnt(8)
	v_mfma_f32_32x32x16_bf16 v[64:79], v[68:71], v[124:127], 0
	v_add_f32_e32 v128, v217, v128
	v_add_f32_e32 v128, v218, v128
	v_add_f32_e32 v128, v212, v128
	v_add_f32_e32 v128, v214, v128
	v_add_f32_e32 v128, v211, v128
	v_add_f32_e32 v128, v213, v128
	v_exp_f32_e32 v138, v138
	s_waitcnt lgkmcnt(7)
	v_mfma_f32_32x32x16_bf16 v[80:95], v[200:203], v[120:123], v[80:95]
	v_add_f32_e32 v128, v208, v128
	v_exp_f32_e32 v139, v139
	v_add_f32_e32 v128, v210, v128
	v_exp_f32_e32 v164, v136
	v_add_f32_e32 v128, v207, v128
	v_exp_f32_e32 v137, v137
	v_add_f32_e32 v128, v209, v128
	s_waitcnt lgkmcnt(6)
	v_mfma_f32_32x32x16_bf16 v[64:79], v[226:229], v[120:123], v[64:79]
	ds_read_b128 v[200:203], v185 offset:49152
	ds_read_b128 v[226:229], v185 offset:57344
	v_exp_f32_e32 v165, v132
	v_add_f32_e32 v128, v138, v128
	v_add_f32_e32 v128, v139, v128
	v_exp_f32_e32 v206, v130
	v_add_f32_e32 v128, v164, v128
	v_exp_f32_e32 v215, v131
	s_waitcnt lgkmcnt(7)
	v_mfma_f32_32x32x16_bf16 v[80:95], v[230:233], v[116:119], v[80:95]
	v_add_f32_e32 v128, v137, v128
	v_add_f32_e32 v128, v165, v128
	v_exp_f32_e32 v225, v129
	v_exp_f32_e32 v162, v162
	v_exp_f32_e32 v163, v163
	v_exp_f32_e32 v160, v160
	v_exp_f32_e32 v161, v161
	s_waitcnt lgkmcnt(6)
	v_mfma_f32_32x32x16_bf16 v[64:79], v[234:237], v[116:119], v[64:79]
	ds_read_b128 v[230:233], v186 offset:49152
	ds_read_b128 v[234:237], v186 offset:57344
	v_cvt_pk_bf16_f32 v129, v220, v223
	v_cvt_pk_bf16_f32 v130, v219, v221
	v_cvt_pk_bf16_f32 v131, v217, v218
	v_cvt_pk_bf16_f32 v132, v212, v214
	v_cvt_pk_bf16_f32 v136, v138, v139
	v_cvt_pk_bf16_f32 v137, v164, v137
	s_waitcnt lgkmcnt(7)
	v_mfma_f32_32x32x16_bf16 v[80:95], v[238:241], v[112:115], v[80:95]
	v_cvt_pk_bf16_f32 v139, v206, v215
	v_permlane32_swap_b32_e32 v129, v131
	s_nop 0
	v_permlane32_swap_b32_e32 v137, v139
	s_waitcnt lgkmcnt(6)
	v_mfma_f32_32x32x16_bf16 v[64:79], v[242:245], v[112:115], v[64:79]
	ds_read_b128 v[238:241], v187 offset:49152
	ds_read_b128 v[242:245], v187 offset:57344
	s_waitcnt lgkmcnt(7)
	v_mfma_f32_32x32x16_bf16 v[80:95], v[246:249], v[108:111], v[80:95]
	s_waitcnt lgkmcnt(6)
	v_mfma_f32_32x32x16_bf16 v[64:79], v[250:253], v[108:111], v[64:79]
	ds_read_b128 v[246:249], v199
	ds_read_b128 v[250:253], v199 offset:4096
	s_waitcnt lgkmcnt(7)
	v_mfma_f32_32x32x16_bf16 v[80:95], v[200:203], v[104:107], v[80:95]
	s_waitcnt lgkmcnt(6)
	v_mfma_f32_32x32x16_bf16 v[64:79], v[226:229], v[104:107], v[64:79]
	ds_read_b128 v[200:203], v204
	ds_read_b128 v[226:229], v204 offset:4096
	v_add_u32_e32 v204, s6, v173
	s_waitcnt lgkmcnt(7)
	v_mfma_f32_32x32x16_bf16 v[80:95], v[230:233], v[100:103], v[80:95]
	s_waitcnt lgkmcnt(6)
	v_mfma_f32_32x32x16_bf16 v[64:79], v[234:237], v[100:103], v[64:79]
	ds_read_b128 v[230:233], v205
	ds_read_b128 v[234:237], v205 offset:4096
	s_waitcnt lgkmcnt(7)
	v_mfma_f32_32x32x16_bf16 v[80:95], v[238:241], v[96:99], v[80:95]
	s_waitcnt lgkmcnt(6)
	v_mfma_f32_32x32x16_bf16 v[64:79], v[242:245], v[96:99], v[64:79]
	ds_read_b128 v[238:241], v204
	ds_read_b128 v[242:245], v204 offset:4096
	s_waitcnt lgkmcnt(7)
	v_mfma_f32_32x32x16_bf16 v[80:95], v[246:249], v[142:145], v[80:95]
	s_waitcnt lgkmcnt(6)
	v_mfma_f32_32x32x16_bf16 v[64:79], v[250:253], v[142:145], v[64:79]
	s_waitcnt lgkmcnt(5)
	v_mfma_f32_32x32x16_bf16 v[80:95], v[200:203], v[146:149], v[80:95]
	s_waitcnt lgkmcnt(4)
	v_mfma_f32_32x32x16_bf16 v[64:79], v[226:229], v[146:149], v[64:79]
	s_waitcnt lgkmcnt(3)
	v_mfma_f32_32x32x16_bf16 v[80:95], v[230:233], v[150:153], v[80:95]
	v_exp_f32_e32 v205, v133
	v_cvt_pk_bf16_f32 v133, v211, v213
	v_cvt_pk_bf16_f32 v138, v165, v205
	v_add_f32_e32 v128, v205, v128
	v_add_f32_e32 v128, v206, v128
	v_add_f32_e32 v128, v215, v128
	s_waitcnt lgkmcnt(2)
	v_mfma_f32_32x32x16_bf16 v[64:79], v[234:237], v[150:153], v[64:79]
	v_add_f32_e32 v128, v216, v128
	v_add_f32_e32 v128, v225, v128
	v_add_f32_e32 v128, v162, v128
	v_add_f32_e32 v128, v163, v128
	v_add_f32_e32 v128, v160, v128
	v_add_f32_e32 v128, v161, v128
	s_waitcnt lgkmcnt(1)
	v_mfma_f32_32x32x16_bf16 v[80:95], v[238:241], v[156:159], v[80:95]
	v_exp_f32_e32 v226, v134
	v_exp_f32_e32 v227, v135
	v_cvt_pk_bf16_f32 v134, v208, v210
	v_cvt_pk_bf16_f32 v135, v207, v209
	v_add_f32_e32 v128, v226, v128
	v_add_f32_e32 v203, v227, v128
	v_mov_b32_e32 v204, v203
	s_waitcnt lgkmcnt(0)
	v_mfma_f32_32x32x16_bf16 v[64:79], v[242:245], v[156:159], v[64:79]
	s_nop 0
	v_permlane32_swap_b32_e32 v203, v204
	v_cvt_pk_bf16_f32 v128, v222, v224
	v_cvt_pk_bf16_f32 v208, v216, v225
	v_cvt_pk_bf16_f32 v209, v162, v163
	v_cvt_pk_bf16_f32 v210, v160, v161
	v_cvt_pk_bf16_f32 v211, v226, v227
	v_permlane32_swap_b32_e32 v132, v134
	v_permlane32_swap_b32_e32 v128, v130
	v_permlane32_swap_b32_e32 v133, v135
	v_permlane32_swap_b32_e32 v136, v138
	v_permlane32_swap_b32_e32 v208, v210
	v_permlane32_swap_b32_e32 v209, v211
	ds_read_b64_tr_b16 v[160:161], v167 offset:0
	ds_read_b64_tr_b16 v[162:163], v167 offset:0x800
	ds_read_b64_tr_b16 v[232:233], v167 offset:0x1000
	ds_read_b64_tr_b16 v[234:235], v167 offset:0x1800
	ds_read_b64_tr_b16 v[236:237], v167 offset:0x2000
	ds_read_b64_tr_b16 v[238:239], v167 offset:0x2800
	ds_read_b64_tr_b16 v[240:241], v167 offset:0x3000
	ds_read_b64_tr_b16 v[242:243], v167 offset:0x3800
	v_max_f32_e32 v164, v81, v81
	v_max_f32_e32 v165, v80, v80
	v_max_f32_e32 v164, v165, v164
	v_max3_f32 v164, v164, v82, v83
	v_max3_f32 v164, v164, v84, v85
	v_max3_f32 v164, v164, v86, v87
	v_max3_f32 v164, v164, v88, v89
	v_max3_f32 v164, v164, v90, v91
	v_max3_f32 v164, v164, v92, v93
	v_max3_f32 v164, v164, v94, v95
	s_waitcnt lgkmcnt(0)
	v_mfma_f32_32x32x16_bf16 v[0:15], v[128:131], v[160:163], v[0:15]
	v_max3_f32 v160, v164, v64, v65
	v_max3_f32 v160, v160, v66, v67
	v_max3_f32 v160, v160, v68, v69
	v_mfma_f32_32x32x16_bf16 v[0:15], v[132:135], v[232:235], v[0:15]
	ds_read_b64_tr_b16 v[232:233], v167 offset:0x200
	ds_read_b64_tr_b16 v[234:235], v167 offset:0xa00
	v_max3_f32 v160, v160, v70, v71
	v_max3_f32 v160, v160, v72, v73
	v_max3_f32 v160, v160, v74, v75
	v_mfma_f32_32x32x16_bf16 v[0:15], v[136:139], v[236:239], v[0:15]
	ds_read_b64_tr_b16 v[236:237], v167 offset:0x1200
	ds_read_b64_tr_b16 v[238:239], v167 offset:0x1a00
	ds_read_b64_tr_b16 v[244:245], v167 offset:0x2200
	ds_read_b64_tr_b16 v[246:247], v167 offset:0x2a00
	ds_read_b64_tr_b16 v[248:249], v167 offset:0x3200
	ds_read_b64_tr_b16 v[250:251], v167 offset:0x3a00
	v_max3_f32 v160, v160, v76, v77
	v_max3_f32 v160, v160, v78, v79
	v_mov_b32_e32 v161, v160
	v_mfma_f32_32x32x16_bf16 v[0:15], v[208:211], v[240:243], v[0:15]
	v_max_f32_e32 v162, v198, v198
	v_permlane32_swap_b32_e32 v160, v161
	v_max_f32_e32 v161, v161, v161
	v_max_f32_e32 v160, v160, v160
	v_max_f32_e32 v160, v160, v161
	s_waitcnt lgkmcnt(0)
	v_mfma_f32_32x32x16_bf16 v[32:47], v[128:131], v[232:235], v[32:47]
	ds_read_b64_tr_b16 v[232:233], v167 offset:0x400
	ds_read_b64_tr_b16 v[234:235], v167 offset:0xc00
	v_sub_f32_e32 v161, v160, v198
	v_max_f32_e32 v160, v162, v160
	v_sub_f32_e32 v162, v198, v160
	v_mul_f32_e32 v162, 0x3dd53b94, v162
	v_exp_f32_e32 v162, v162
	v_mfma_f32_32x32x16_bf16 v[32:47], v[132:135], v[236:239], v[32:47]
	ds_read_b64_tr_b16 v[236:237], v167 offset:0x1400
	ds_read_b64_tr_b16 v[238:239], v167 offset:0x1c00
	ds_read_b64_tr_b16 v[240:241], v167 offset:0x2400
	ds_read_b64_tr_b16 v[242:243], v167 offset:0x2c00
	v_cmp_ge_f32_e32 vcc, s46, v161
	s_cmp_eq_u64 vcc, exec
	s_cselect_b64 s[6:7], -1, 0
	v_cndmask_b32_e64 v206, v162, 1.0, s[6:7]
	v_cndmask_b32_e64 v160, v160, v198, s[6:7]
	v_mul_f32_e32 v205, 0xbdd53b94, v160
	v_cmp_gt_f32_e32 vcc, 1.0, v206
	v_mfma_f32_32x32x16_bf16 v[32:47], v[136:139], v[244:247], v[32:47]
	ds_read_b64_tr_b16 v[244:245], v167 offset:0x3400
	ds_read_b64_tr_b16 v[246:247], v167 offset:0x3c00
	v_fmamk_f32 v87, v87, 0x3dd53b94, v205
	v_fmamk_f32 v80, v80, 0x3dd53b94, v205
	v_fmamk_f32 v81, v81, 0x3dd53b94, v205
	v_fmamk_f32 v82, v82, 0x3dd53b94, v205
	v_fmamk_f32 v83, v83, 0x3dd53b94, v205
	v_mfma_f32_32x32x16_bf16 v[32:47], v[208:211], v[248:251], v[32:47]
	v_fmamk_f32 v84, v84, 0x3dd53b94, v205
	v_fmamk_f32 v85, v85, 0x3dd53b94, v205
	v_fmamk_f32 v86, v86, 0x3dd53b94, v205
	v_fmamk_f32 v88, v88, 0x3dd53b94, v205
	v_fmamk_f32 v89, v89, 0x3dd53b94, v205
	s_waitcnt lgkmcnt(0)
	v_mfma_f32_32x32x16_bf16 v[16:31], v[128:131], v[232:235], v[16:31]
	ds_read_b64_tr_b16 v[232:233], v167 offset:0x600
	ds_read_b64_tr_b16 v[234:235], v167 offset:0xe00
	v_fmamk_f32 v90, v90, 0x3dd53b94, v205
	v_fmamk_f32 v91, v91, 0x3dd53b94, v205
	v_fmamk_f32 v92, v92, 0x3dd53b94, v205
	v_fmamk_f32 v93, v93, 0x3dd53b94, v205
	v_fmamk_f32 v94, v94, 0x3dd53b94, v205
	v_mfma_f32_32x32x16_bf16 v[16:31], v[132:135], v[236:239], v[16:31]
	ds_read_b64_tr_b16 v[236:237], v167 offset:0x1600
	ds_read_b64_tr_b16 v[238:239], v167 offset:0x1e00
	v_fmamk_f32 v95, v95, 0x3dd53b94, v205
	v_fmamk_f32 v215, v64, 0x3dd53b94, v205
	v_fmamk_f32 v216, v65, 0x3dd53b94, v205
	v_fmamk_f32 v217, v66, 0x3dd53b94, v205
	v_fmamk_f32 v218, v67, 0x3dd53b94, v205
	v_mfma_f32_32x32x16_bf16 v[16:31], v[136:139], v[240:243], v[16:31]
	ds_read_b64_tr_b16 v[240:241], v167 offset:0x2600
	ds_read_b64_tr_b16 v[242:243], v167 offset:0x2e00
	ds_read_b64_tr_b16 v[248:249], v167 offset:0x3600
	ds_read_b64_tr_b16 v[250:251], v167 offset:0x3e00
	v_fmamk_f32 v219, v68, 0x3dd53b94, v205
	v_fmamk_f32 v212, v73, 0x3dd53b94, v205
	v_fmamk_f32 v213, v74, 0x3dd53b94, v205
	v_fmamk_f32 v214, v75, 0x3dd53b94, v205
	v_mfma_f32_32x32x16_bf16 v[16:31], v[208:211], v[244:247], v[16:31]
	v_fmamk_f32 v207, v76, 0x3dd53b94, v205
	v_fmamk_f32 v220, v77, 0x3dd53b94, v205
	v_fmamk_f32 v221, v78, 0x3dd53b94, v205
	s_waitcnt lgkmcnt(0)
	v_mfma_f32_32x32x16_bf16 v[48:63], v[128:131], v[232:235], v[48:63]
	v_exp_f32_e32 v128, v80
	v_exp_f32_e32 v129, v82
	v_exp_f32_e32 v130, v84
	v_exp_f32_e32 v131, v86
	v_mfma_f32_32x32x16_bf16 v[48:63], v[132:135], v[236:239], v[48:63]
	v_exp_f32_e32 v132, v88
	v_exp_f32_e32 v133, v90
	v_exp_f32_e32 v134, v92
	v_exp_f32_e32 v135, v94
	v_mfma_f32_32x32x16_bf16 v[48:63], v[136:139], v[240:243], v[48:63]
	v_exp_f32_e32 v139, v89
	v_exp_f32_e32 v138, v91
	v_exp_f32_e32 v137, v93
	v_exp_f32_e32 v136, v95
	v_mfma_f32_32x32x16_bf16 v[48:63], v[208:211], v[248:251], v[48:63]
	v_exp_f32_e32 v161, v87
	v_exp_f32_e32 v198, v81
	v_exp_f32_e32 v163, v83
	v_exp_f32_e32 v162, v85
	v_fmamk_f32 v208, v69, 0x3dd53b94, v205
	v_fmamk_f32 v209, v70, 0x3dd53b94, v205
	v_fmamk_f32 v210, v71, 0x3dd53b94, v205
	v_fmamk_f32 v211, v72, 0x3dd53b94, v205
	v_fmac_f32_e32 v205, 0x3dd53b94, v79
	s_cbranch_vccz .LBB0_2016
	s_and_saveexec_b64 s[10:11], s[4:5]
	ds_write_b32 v189, v206 offset:128
	s_or_b64 exec, exec, s[10:11]
	s_waitcnt lgkmcnt(0)
	v_add_u32_e32 v248, s12, v169
	ds_read_b128 v[232:235], v248 offset:224
	ds_read_b128 v[236:239], v248 offset:192
	ds_read_b128 v[240:243], v248 offset:160
	ds_read_b128 v[244:247], v248 offset:128
	s_waitcnt lgkmcnt(3)
	v_pk_mul_f32 v[12:13], v[12:13], v[232:233]
	s_waitcnt lgkmcnt(2)
	v_pk_mul_f32 v[8:9], v[8:9], v[236:237]
	s_waitcnt lgkmcnt(1)
	v_pk_mul_f32 v[4:5], v[4:5], v[240:241]
	v_pk_mul_f32 v[14:15], v[14:15], v[234:235]
	v_pk_mul_f32 v[10:11], v[10:11], v[238:239]
	v_pk_mul_f32 v[6:7], v[6:7], v[242:243]
	s_waitcnt lgkmcnt(0)
	v_pk_mul_f32 v[2:3], v[2:3], v[246:247]
	v_pk_mul_f32 v[0:1], v[0:1], v[244:245]
	v_pk_mul_f32 v[44:45], v[44:45], v[232:233]
	v_pk_mul_f32 v[40:41], v[40:41], v[236:237]
	v_pk_mul_f32 v[36:37], v[36:37], v[240:241]
	v_pk_mul_f32 v[46:47], v[46:47], v[234:235]
	v_pk_mul_f32 v[42:43], v[42:43], v[238:239]
	v_pk_mul_f32 v[38:39], v[38:39], v[242:243]
	v_pk_mul_f32 v[34:35], v[34:35], v[246:247]
	v_pk_mul_f32 v[32:33], v[32:33], v[244:245]
	v_pk_mul_f32 v[28:29], v[28:29], v[232:233]
	v_pk_mul_f32 v[24:25], v[24:25], v[236:237]
	v_pk_mul_f32 v[20:21], v[20:21], v[240:241]
	v_pk_mul_f32 v[30:31], v[30:31], v[234:235]
	v_pk_mul_f32 v[26:27], v[26:27], v[238:239]
	v_pk_mul_f32 v[22:23], v[22:23], v[242:243]
	v_pk_mul_f32 v[18:19], v[18:19], v[246:247]
	v_pk_mul_f32 v[16:17], v[16:17], v[244:245]
	v_pk_mul_f32 v[60:61], v[60:61], v[232:233]
	v_pk_mul_f32 v[56:57], v[56:57], v[236:237]
	v_pk_mul_f32 v[52:53], v[52:53], v[240:241]
	v_pk_mul_f32 v[62:63], v[62:63], v[234:235]
	v_pk_mul_f32 v[58:59], v[58:59], v[238:239]
	v_pk_mul_f32 v[54:55], v[54:55], v[242:243]
	v_pk_mul_f32 v[50:51], v[50:51], v[246:247]
	v_pk_mul_f32 v[48:49], v[48:49], v[244:245]
.LBB0_2016:
	s_waitcnt vmcnt(0) lgkmcnt(0)
	s_barrier
	s_add_i32 s80, s13, 64
	s_cmp_lt_u32 s8, 2
	s_cselect_b32 s80, s80, s14
	s_mul_i32 s81, s80, 0xc00
	s_add_i32 s85, s82, 0xc000
	s_mov_b32 m0, s85
	s_add_i32 s85, s82, 0x12000
	buffer_load_dwordx4 v154, s[72:75], s81 offen lds
	s_mov_b32 m0, s85
	s_add_i32 s85, s82, 0xe000
	buffer_load_dwordx4 v155, s[72:75], s81 offen lds
	s_mov_b32 m0, s85
	s_add_i32 s81, s81, 0x18000
	buffer_load_dwordx4 v154, s[72:75], s81 offen lds
	s_lshl_b32 s81, s84, 11
	s_add_i32 s85, s82, 0x0
	s_mov_b32 m0, s85
	s_add_i32 s85, s82, 0x2000
	buffer_load_dwordx4 v196, s[76:79], s81 offen lds
	s_mov_b32 m0, s85
	s_add_i32 s81, s81, 0x10000
	buffer_load_dwordx4 v196, s[76:79], s81 offen lds
	s_mov_b32 s83, s80
	ds_read_b128 v[64:67], v180 offset:32768
	ds_read_b128 v[68:71], v180 offset:40960
	ds_read_b128 v[222:225], v181 offset:32768
	ds_read_b128 v[226:229], v181 offset:40960
	ds_read_b128 v[230:233], v182 offset:32768
	ds_read_b128 v[234:237], v182 offset:40960
	ds_read_b128 v[238:241], v183 offset:32768
	ds_read_b128 v[242:245], v183 offset:40960
	ds_read_b128 v[246:249], v184 offset:32768
	ds_read_b128 v[250:253], v184 offset:40960
	v_exp_f32_e32 v164, v215
	v_add_f32_e32 v215, 0, v128
	s_waitcnt lgkmcnt(9)
	v_mfma_f32_32x32x16_bf16 v[80:95], v[64:67], v[124:127], 0
	v_add_f32_e32 v215, v198, v215
	v_add_f32_e32 v215, v129, v215
	v_add_f32_e32 v215, v163, v215
	v_add_f32_e32 v215, v130, v215
	v_add_f32_e32 v215, v162, v215
	v_add_f32_e32 v215, v131, v215
	v_add_f32_e32 v215, v161, v215
	s_waitcnt lgkmcnt(8)
	v_mfma_f32_32x32x16_bf16 v[64:79], v[68:71], v[124:127], 0
	v_add_f32_e32 v215, v132, v215
	v_add_f32_e32 v215, v139, v215
	v_add_f32_e32 v215, v133, v215
	v_add_f32_e32 v215, v138, v215
	v_add_f32_e32 v215, v134, v215
	v_exp_f32_e32 v165, v216
	v_add_f32_e32 v215, v137, v215
	s_waitcnt lgkmcnt(7)
	v_mfma_f32_32x32x16_bf16 v[80:95], v[222:225], v[120:123], v[80:95]
	v_exp_f32_e32 v217, v217
	v_add_f32_e32 v215, v135, v215
	v_exp_f32_e32 v218, v218
	v_add_f32_e32 v215, v136, v215
	v_exp_f32_e32 v219, v219
	v_add_f32_e32 v215, v164, v215
	v_exp_f32_e32 v208, v208
	s_waitcnt lgkmcnt(6)
	v_mfma_f32_32x32x16_bf16 v[64:79], v[226:229], v[120:123], v[64:79]
	ds_read_b128 v[222:225], v185 offset:32768
	ds_read_b128 v[226:229], v185 offset:40960
	v_add_f32_e32 v215, v165, v215
	v_exp_f32_e32 v209, v209
	v_add_f32_e32 v215, v217, v215
	v_exp_f32_e32 v210, v210
	v_add_f32_e32 v215, v218, v215
	v_exp_f32_e32 v211, v211
	s_waitcnt lgkmcnt(7)
	v_mfma_f32_32x32x16_bf16 v[80:95], v[230:233], v[116:119], v[80:95]
	v_add_f32_e32 v215, v219, v215
	v_exp_f32_e32 v212, v212
	v_add_f32_e32 v215, v208, v215
	v_exp_f32_e32 v213, v213
	v_add_f32_e32 v215, v209, v215
	v_exp_f32_e32 v214, v214
	v_add_f32_e32 v215, v210, v215
	s_waitcnt lgkmcnt(6)
	v_mfma_f32_32x32x16_bf16 v[64:79], v[234:237], v[116:119], v[64:79]
	ds_read_b128 v[230:233], v186 offset:32768
	ds_read_b128 v[234:237], v186 offset:40960
	v_exp_f32_e32 v207, v207
	v_add_f32_e32 v215, v211, v215
	v_exp_f32_e32 v220, v220
	v_add_f32_e32 v215, v212, v215
	v_exp_f32_e32 v221, v221
	v_add_f32_e32 v215, v213, v215
	s_waitcnt lgkmcnt(7)
	v_mfma_f32_32x32x16_bf16 v[80:95], v[238:241], v[112:115], v[80:95]
	v_exp_f32_e32 v205, v205
	v_add_f32_e32 v215, v214, v215
	v_add_f32_e32 v215, v207, v215
	v_add_f32_e32 v215, v220, v215
	v_add_f32_e32 v215, v221, v215
	v_add_f32_e32 v215, v205, v215
	v_mov_b32_e32 v216, v215
	s_waitcnt lgkmcnt(6)
	v_mfma_f32_32x32x16_bf16 v[64:79], v[242:245], v[112:115], v[64:79]
	ds_read_b128 v[238:241], v187 offset:32768
	ds_read_b128 v[242:245], v187 offset:40960
	v_permlane32_swap_b32_e32 v215, v216
	v_cvt_pk_bf16_f32 v128, v128, v198
	v_cvt_pk_bf16_f32 v129, v129, v163
	v_cvt_pk_bf16_f32 v130, v130, v162
	v_cvt_pk_bf16_f32 v131, v131, v161
	s_waitcnt lgkmcnt(7)
	v_mfma_f32_32x32x16_bf16 v[80:95], v[246:249], v[108:111], v[80:95]
	v_cvt_pk_bf16_f32 v132, v132, v139
	v_cvt_pk_bf16_f32 v133, v133, v138
	v_cvt_pk_bf16_f32 v134, v134, v137
	v_cvt_pk_bf16_f32 v135, v135, v136
	v_cvt_pk_bf16_f32 v136, v164, v165
	v_cvt_pk_bf16_f32 v137, v217, v218
	v_cvt_pk_bf16_f32 v138, v219, v208
	s_waitcnt lgkmcnt(6)
	v_mfma_f32_32x32x16_bf16 v[64:79], v[250:253], v[108:111], v[64:79]
	ds_read_b128 v[246:249], v191
	ds_read_b128 v[250:253], v191 offset:4096
	v_cvt_pk_bf16_f32 v139, v209, v210
	v_cvt_pk_bf16_f32 v208, v211, v212
	v_cvt_pk_bf16_f32 v209, v213, v214
	v_cvt_pk_bf16_f32 v210, v207, v220
	v_cvt_pk_bf16_f32 v211, v221, v205
	v_permlane32_swap_b32_e32 v128, v130
	s_waitcnt lgkmcnt(7)
	v_mfma_f32_32x32x16_bf16 v[80:95], v[222:225], v[104:107], v[80:95]
	v_permlane32_swap_b32_e32 v129, v131
	v_permlane32_swap_b32_e32 v132, v134
	v_permlane32_swap_b32_e32 v133, v135
	v_permlane32_swap_b32_e32 v136, v138
	s_waitcnt lgkmcnt(6)
	v_mfma_f32_32x32x16_bf16 v[64:79], v[226:229], v[104:107], v[64:79]
	ds_read_b128 v[222:225], v192
	ds_read_b128 v[226:229], v192 offset:4096
	v_permlane32_swap_b32_e32 v137, v139
	v_permlane32_swap_b32_e32 v208, v210
	v_permlane32_swap_b32_e32 v209, v211
	s_waitcnt lgkmcnt(7)
	v_mfma_f32_32x32x16_bf16 v[80:95], v[230:233], v[100:103], v[80:95]
	s_waitcnt lgkmcnt(6)
	v_mfma_f32_32x32x16_bf16 v[64:79], v[234:237], v[100:103], v[64:79]
	ds_read_b128 v[230:233], v193
	ds_read_b128 v[234:237], v193 offset:4096
	s_waitcnt lgkmcnt(7)
	v_mfma_f32_32x32x16_bf16 v[80:95], v[238:241], v[96:99], v[80:95]
	s_waitcnt lgkmcnt(6)
	v_mfma_f32_32x32x16_bf16 v[64:79], v[242:245], v[96:99], v[64:79]
	ds_read_b128 v[238:241], v194
	ds_read_b128 v[242:245], v194 offset:4096
	s_waitcnt lgkmcnt(7)
	v_mfma_f32_32x32x16_bf16 v[80:95], v[246:249], v[142:145], v[80:95]
	s_waitcnt lgkmcnt(6)
	v_mfma_f32_32x32x16_bf16 v[64:79], v[250:253], v[142:145], v[64:79]
	s_waitcnt lgkmcnt(5)
	v_mfma_f32_32x32x16_bf16 v[80:95], v[222:225], v[146:149], v[80:95]
	s_waitcnt lgkmcnt(4)
	v_mfma_f32_32x32x16_bf16 v[64:79], v[226:229], v[146:149], v[64:79]
	s_waitcnt lgkmcnt(3)
	v_mfma_f32_32x32x16_bf16 v[80:95], v[230:233], v[150:153], v[80:95]
	s_waitcnt lgkmcnt(2)
	v_mfma_f32_32x32x16_bf16 v[64:79], v[234:237], v[150:153], v[64:79]
	s_waitcnt lgkmcnt(1)
	v_mfma_f32_32x32x16_bf16 v[80:95], v[238:241], v[156:159], v[80:95]
	s_waitcnt lgkmcnt(0)
	v_mfma_f32_32x32x16_bf16 v[64:79], v[242:245], v[156:159], v[64:79]
	ds_read_b64_tr_b16 v[238:239], v174 offset:0
	ds_read_b64_tr_b16 v[240:241], v174 offset:0x800
	ds_read_b64_tr_b16 v[242:243], v174 offset:0x1000
	ds_read_b64_tr_b16 v[244:245], v174 offset:0x1800
	ds_read_b64_tr_b16 v[246:247], v174 offset:0x2000
	ds_read_b64_tr_b16 v[248:249], v174 offset:0x2800
	ds_read_b64_tr_b16 v[250:251], v174 offset:0x3000
	ds_read_b64_tr_b16 v[252:253], v174 offset:0x3800
	s_nop 3
	v_max_f32_e32 v161, v81, v81
	v_max_f32_e32 v162, v80, v80
	v_max_f32_e32 v161, v162, v161
	v_max3_f32 v161, v161, v82, v83
	v_max3_f32 v161, v161, v84, v85
	v_max3_f32 v161, v161, v86, v87
	v_max3_f32 v161, v161, v88, v89
	v_max3_f32 v161, v161, v90, v91
	v_max3_f32 v161, v161, v92, v93
	v_max3_f32 v161, v161, v94, v95
	s_waitcnt lgkmcnt(0)
	v_mfma_f32_32x32x16_bf16 v[0:15], v[128:131], v[238:241], v[0:15]
	ds_read_b64_tr_b16 v[238:239], v174 offset:0x200
	ds_read_b64_tr_b16 v[240:241], v174 offset:0xa00
	v_max3_f32 v161, v161, v64, v65
	v_max3_f32 v161, v161, v66, v67
	v_max3_f32 v161, v161, v68, v69
	v_mfma_f32_32x32x16_bf16 v[0:15], v[132:135], v[242:245], v[0:15]
	ds_read_b64_tr_b16 v[242:243], v174 offset:0x1200
	ds_read_b64_tr_b16 v[244:245], v174 offset:0x1a00
	v_max3_f32 v161, v161, v70, v71
	v_max3_f32 v161, v161, v72, v73
	v_max3_f32 v161, v161, v74, v75
	v_mfma_f32_32x32x16_bf16 v[0:15], v[136:139], v[246:249], v[0:15]
	ds_read_b64_tr_b16 v[246:247], v174 offset:0x2200
	ds_read_b64_tr_b16 v[248:249], v174 offset:0x2a00
	ds_read_b64_tr_b16 v[162:163], v174 offset:0x3200
	ds_read_b64_tr_b16 v[164:165], v174 offset:0x3a00
	v_max3_f32 v161, v161, v76, v77
	v_max3_f32 v161, v161, v78, v79
	v_mov_b32_e32 v198, v161
	v_mfma_f32_32x32x16_bf16 v[0:15], v[208:211], v[250:253], v[0:15]
	v_max_f32_e32 v205, v160, v160
	v_permlane32_swap_b32_e32 v161, v198
	v_max_f32_e32 v198, v198, v198
	v_max_f32_e32 v161, v161, v161
	v_max_f32_e32 v161, v161, v198
	s_waitcnt lgkmcnt(0)
	v_mfma_f32_32x32x16_bf16 v[32:47], v[128:131], v[238:241], v[32:47]
	ds_read_b64_tr_b16 v[238:239], v174 offset:0x400
	ds_read_b64_tr_b16 v[240:241], v174 offset:0xc00
	v_sub_f32_e32 v198, v161, v160
	v_max_f32_e32 v161, v205, v161
	v_sub_f32_e32 v205, v160, v161
	v_mul_f32_e32 v205, 0x3dd53b94, v205
	v_exp_f32_e32 v205, v205
	v_mfma_f32_32x32x16_bf16 v[32:47], v[132:135], v[242:245], v[32:47]
	ds_read_b64_tr_b16 v[242:243], v174 offset:0x1400
	ds_read_b64_tr_b16 v[244:245], v174 offset:0x1c00
	v_cmp_ge_f32_e32 vcc, s46, v198
	s_cmp_eq_u64 vcc, exec
	s_cselect_b64 s[6:7], -1, 0
	v_cndmask_b32_e64 v205, v205, 1.0, s[6:7]
	v_cndmask_b32_e64 v198, v161, v160, s[6:7]
	v_mul_f32_e32 v236, 0xbdd53b94, v198
	v_mov_b32_e32 v237, v236
	v_cmp_gt_f32_e32 vcc, 1.0, v205
	v_mfma_f32_32x32x16_bf16 v[32:47], v[136:139], v[246:249], v[32:47]
	ds_read_b64_tr_b16 v[246:247], v174 offset:0x2400
	ds_read_b64_tr_b16 v[248:249], v174 offset:0x2c00
	ds_read_b64_tr_b16 v[250:251], v174 offset:0x3400
	ds_read_b64_tr_b16 v[252:253], v174 offset:0x3c00
	v_fmamk_f32 v80, v80, 0x3dd53b94, v236
	v_fmamk_f32 v81, v81, 0x3dd53b94, v236
	v_fmamk_f32 v82, v82, 0x3dd53b94, v236
	v_fmamk_f32 v83, v83, 0x3dd53b94, v236
	v_mfma_f32_32x32x16_bf16 v[32:47], v[208:211], v[162:165], v[32:47]
	v_fmamk_f32 v84, v84, 0x3dd53b94, v236
	v_fmamk_f32 v85, v85, 0x3dd53b94, v236
	v_fmamk_f32 v86, v86, 0x3dd53b94, v236
	v_fmamk_f32 v87, v87, 0x3dd53b94, v236
	s_waitcnt lgkmcnt(0)
	v_mfma_f32_32x32x16_bf16 v[16:31], v[128:131], v[238:241], v[16:31]
	ds_read_b64_tr_b16 v[162:163], v174 offset:0x600
	ds_read_b64_tr_b16 v[164:165], v174 offset:0xe00
	ds_read_b64_tr_b16 v[238:239], v174 offset:0x1600
	ds_read_b64_tr_b16 v[240:241], v174 offset:0x1e00
	v_fmamk_f32 v88, v88, 0x3dd53b94, v236
	v_fmamk_f32 v89, v89, 0x3dd53b94, v236
	v_fmamk_f32 v90, v90, 0x3dd53b94, v236
	v_fmamk_f32 v91, v91, 0x3dd53b94, v236
	v_mfma_f32_32x32x16_bf16 v[16:31], v[132:135], v[242:245], v[16:31]
	ds_read_b64_tr_b16 v[242:243], v174 offset:0x2600
	ds_read_b64_tr_b16 v[244:245], v174 offset:0x2e00
	v_fmamk_f32 v92, v92, 0x3dd53b94, v236
	v_fmamk_f32 v93, v93, 0x3dd53b94, v236
	v_fmamk_f32 v94, v94, 0x3dd53b94, v236
	v_fmamk_f32 v95, v95, 0x3dd53b94, v236
	v_mfma_f32_32x32x16_bf16 v[16:31], v[136:139], v[246:249], v[16:31]
	ds_read_b64_tr_b16 v[246:247], v174 offset:0x3600
	ds_read_b64_tr_b16 v[248:249], v174 offset:0x3e00
	v_exp_f32_e32 v222, v80
	v_exp_f32_e32 v224, v81
	v_exp_f32_e32 v220, v82
	v_mfma_f32_32x32x16_bf16 v[16:31], v[208:211], v[250:253], v[16:31]
	v_exp_f32_e32 v223, v83
	v_exp_f32_e32 v219, v84
	v_exp_f32_e32 v221, v85
	s_waitcnt lgkmcnt(0)
	v_mfma_f32_32x32x16_bf16 v[48:63], v[128:131], v[162:165], v[48:63]
	v_exp_f32_e32 v217, v86
	v_exp_f32_e32 v218, v87
	v_exp_f32_e32 v212, v88
	v_pk_fma_f32 v[130:131], v[70:71], s[26:27], v[236:237] op_sel_hi:[1,0,0]
	v_pk_fma_f32 v[128:129], v[72:73], s[26:27], v[236:237] op_sel_hi:[1,0,0]
	v_mfma_f32_32x32x16_bf16 v[48:63], v[132:135], v[238:241], v[48:63]
	v_exp_f32_e32 v214, v89
	v_exp_f32_e32 v213, v91
	v_exp_f32_e32 v207, v94
	v_pk_fma_f32 v[132:133], v[68:69], s[26:27], v[236:237] op_sel_hi:[1,0,0]
	v_pk_fma_f32 v[134:135], v[78:79], s[26:27], v[236:237] op_sel_hi:[1,0,0]
	v_mfma_f32_32x32x16_bf16 v[48:63], v[136:139], v[242:245], v[48:63]
	v_pk_fma_f32 v[138:139], v[64:65], s[26:27], v[236:237] op_sel_hi:[1,0,0]
	v_pk_fma_f32 v[136:137], v[66:67], s[26:27], v[236:237] op_sel_hi:[1,0,0]
	v_pk_fma_f32 v[162:163], v[74:75], s[26:27], v[236:237] op_sel_hi:[1,0,0]
	v_pk_fma_f32 v[160:161], v[76:77], s[26:27], v[236:237] op_sel_hi:[1,0,0]
	v_mfma_f32_32x32x16_bf16 v[48:63], v[208:211], v[246:249], v[48:63]
	v_exp_f32_e32 v211, v90
	v_exp_f32_e32 v208, v92
	v_exp_f32_e32 v210, v93
	v_exp_f32_e32 v209, v95
	v_add_f32_e32 v64, v203, v204
	v_fmac_f32_e32 v64, v197, v140
	v_add_f32_e32 v140, v215, v216
	s_addk_i32 s13, 0x80
	s_addk_i32 s14, 0x80
	v_fmac_f32_e32 v140, v64, v206
	s_cbranch_vccz .LBB0_2020
	s_and_saveexec_b64 s[10:11], s[4:5]
	ds_write_b32 v189, v205 offset:128
	s_or_b64 exec, exec, s[10:11]
	s_waitcnt lgkmcnt(0)
	v_add_u32_e32 v164, s12, v169
	ds_read_b128 v[238:241], v164 offset:224
	ds_read_b128 v[242:245], v164 offset:192
	ds_read_b128 v[246:249], v164 offset:160
	ds_read_b128 v[250:253], v164 offset:128
	s_waitcnt lgkmcnt(3)
	v_pk_mul_f32 v[12:13], v[12:13], v[238:239]
	s_waitcnt lgkmcnt(2)
	v_pk_mul_f32 v[8:9], v[8:9], v[242:243]
	s_waitcnt lgkmcnt(1)
	v_pk_mul_f32 v[4:5], v[4:5], v[246:247]
	v_pk_mul_f32 v[14:15], v[14:15], v[240:241]
	v_pk_mul_f32 v[10:11], v[10:11], v[244:245]
	v_pk_mul_f32 v[6:7], v[6:7], v[248:249]
	s_waitcnt lgkmcnt(0)
	v_pk_mul_f32 v[2:3], v[2:3], v[252:253]
	v_pk_mul_f32 v[0:1], v[0:1], v[250:251]
	v_pk_mul_f32 v[44:45], v[44:45], v[238:239]
	v_pk_mul_f32 v[40:41], v[40:41], v[242:243]
	v_pk_mul_f32 v[36:37], v[36:37], v[246:247]
	v_pk_mul_f32 v[46:47], v[46:47], v[240:241]
	v_pk_mul_f32 v[42:43], v[42:43], v[244:245]
	v_pk_mul_f32 v[38:39], v[38:39], v[248:249]
	v_pk_mul_f32 v[34:35], v[34:35], v[252:253]
	v_pk_mul_f32 v[32:33], v[32:33], v[250:251]
	v_pk_mul_f32 v[28:29], v[28:29], v[238:239]
	v_pk_mul_f32 v[24:25], v[24:25], v[242:243]
	v_pk_mul_f32 v[20:21], v[20:21], v[246:247]
	v_pk_mul_f32 v[30:31], v[30:31], v[240:241]
	v_pk_mul_f32 v[26:27], v[26:27], v[244:245]
	v_pk_mul_f32 v[22:23], v[22:23], v[248:249]
	v_pk_mul_f32 v[18:19], v[18:19], v[252:253]
	v_pk_mul_f32 v[16:17], v[16:17], v[250:251]
	v_pk_mul_f32 v[60:61], v[60:61], v[238:239]
	v_pk_mul_f32 v[56:57], v[56:57], v[242:243]
	v_pk_mul_f32 v[52:53], v[52:53], v[246:247]
	v_pk_mul_f32 v[62:63], v[62:63], v[240:241]
	v_pk_mul_f32 v[58:59], v[58:59], v[244:245]
	v_pk_mul_f32 v[54:55], v[54:55], v[248:249]
	v_pk_mul_f32 v[50:51], v[50:51], v[252:253]
	v_pk_mul_f32 v[48:49], v[48:49], v[250:251]
